# grid barrier: the last-arriving XCD leader releases every XCD generation word directly, other leaders wait on their own XCD word (removes the TOPGEN hop)
# speedup vs baseline: 1.0046x; 1.0046x over previous
.LBB0_81:
	s_or_b64 exec, exec, s[10:11]
	v_cvt_f32_u32_e32 v5, v3
	s_waitcnt vmcnt(0)
	v_readfirstlane_b32 s3, v4
	v_sub_u32_e32 v4, 0, v3
	v_rcp_iflag_f32_e32 v5, v5
	v_add_u32_e32 v6, s3, v2
	v_mul_f32_e32 v5, 0x4f7ffffe, v5
	v_cvt_u32_f32_e32 v5, v5
	v_mul_lo_u32 v2, v4, v5
	v_mul_hi_u32 v2, v5, v2
	v_add_u32_e32 v2, v5, v2
	v_mul_hi_u32 v2, v6, v2
	v_mul_lo_u32 v4, v2, v3
	v_sub_u32_e32 v4, v6, v4
	v_add_u32_e32 v5, 1, v2
	v_cmp_ge_u32_e32 vcc, v4, v3
	s_nop 1
	v_cndmask_b32_e32 v2, v2, v5, vcc
	v_sub_u32_e32 v5, v4, v3
	v_cndmask_b32_e32 v4, v4, v5, vcc
	v_add_u32_e32 v5, 1, v2
	v_cmp_ge_u32_e32 vcc, v4, v3
	v_add_u32_e32 v4, 1, v6
	s_nop 0
	v_cndmask_b32_e32 v2, v2, v5, vcc
	v_mul_lo_u32 v5, v3, v2
	v_add_u32_e32 v3, v5, v3
	v_cmp_ne_u32_e32 vcc, v4, v3
	v_readfirstlane_b32 s98, v2
	s_and_saveexec_b64 s[8:9], vcc
	s_xor_b64 s[8:9], exec, s[8:9]
	s_cbranch_execz .LBB0_95
	s_waitcnt lgkmcnt(0)
	v_mov_b32_e32 v1, 0x2000
	global_load_dword v1, v1, s[6:7] offset:1024 sc1
	s_add_u32 s20, s6, 0x2400
	s_addc_u32 s21, s7, 0
	s_waitcnt vmcnt(0)
	v_cmp_eq_u32_e32 vcc, v1, v2
	s_and_saveexec_b64 s[10:11], vcc
	s_cbranch_execz .LBB0_94
	s_mov_b32 s3, 1
	s_mov_b64 s[24:25], 0
	v_mov_b32_e32 v1, 0
	s_branch .LBB0_85

.LBB0_98:
	s_or_b64 exec, exec, s[10:11]
	v_cvt_f32_u32_e32 v4, v1
	s_waitcnt vmcnt(0)
	v_readfirstlane_b32 s3, v3
	s_add_u32 s10, s60, 0x3500
	s_addc_u32 s11, s61, 0
	v_rcp_iflag_f32_e32 v4, v4
	v_add_u32_e32 v2, s3, v2
	v_add_u32_e32 v5, 1, v2
	s_mov_b64 s[20:21], -1
	v_mul_f32_e32 v3, 0x4f7ffffe, v4
	v_cvt_u32_f32_e32 v3, v3
	v_sub_u32_e32 v4, 0, v1
	v_mul_lo_u32 v4, v4, v3
	v_mul_hi_u32 v4, v3, v4
	v_add_u32_e32 v3, v3, v4
	v_mul_hi_u32 v3, v2, v3
	v_mul_lo_u32 v4, v3, v1
	v_sub_u32_e32 v2, v2, v4
	v_add_u32_e32 v6, 1, v3
	v_cmp_ge_u32_e32 vcc, v2, v1
	v_sub_u32_e32 v4, v2, v1
	s_nop 0
	v_cndmask_b32_e32 v3, v3, v6, vcc
	v_cndmask_b32_e32 v2, v2, v4, vcc
	v_add_u32_e32 v4, 1, v3
	v_cmp_ge_u32_e32 vcc, v2, v1
	s_nop 1
	v_cndmask_b32_e32 v4, v3, v4, vcc
	v_mul_lo_u32 v2, v1, v4
	v_add_u32_e32 v1, v2, v1
	v_cmp_ne_u32_e32 vcc, v5, v1
	v_mov_b64_e32 v[2:3], s[10:11]
	s_and_b64 vcc, exec, vcc
	s_cbranch_vccz .Lxb_last_0
	v_mov_b32_e32 v1, 0x2000
	s_mov_b32 s99, 0
.Lxb_spin_0:
	global_load_dword v2, v1, s[6:7] offset:1024 sc1
	s_add_u32 s99, s99, 1
	s_waitcnt vmcnt(0)
	v_readfirstlane_b32 s100, v2
	s_cmp_lg_u32 s100, s98
	s_cbranch_scc1 .Lxb_done_0
	s_cmp_gt_u32 s99, 0x40000
	s_cbranch_scc1 .Lxb_done_0
	s_sleep 1
	s_branch .Lxb_spin_0
.Lxb_last_0:
	v_mov_b32_e32 v1, 0x2000
	v_mov_b32_e32 v2, 1
	global_atomic_add v1, v2, s[60:61] offset:1024
	global_atomic_add v1, v2, s[60:61] offset:1280
	global_atomic_add v1, v2, s[60:61] offset:1536
	global_atomic_add v1, v2, s[60:61] offset:1792
	global_atomic_add v1, v2, s[60:61] offset:2048
	global_atomic_add v1, v2, s[60:61] offset:2304
	global_atomic_add v1, v2, s[60:61] offset:2560
	global_atomic_add v1, v2, s[60:61] offset:2816
	v_mov_b32_e32 v1, 0x2800
	global_atomic_add v1, v2, s[60:61] offset:1024
	global_atomic_add v1, v2, s[60:61] offset:1280
	global_atomic_add v1, v2, s[60:61] offset:1536
	global_atomic_add v1, v2, s[60:61] offset:1792
	global_atomic_add v1, v2, s[60:61] offset:2048
	global_atomic_add v1, v2, s[60:61] offset:2304
	global_atomic_add v1, v2, s[60:61] offset:2560
	global_atomic_add v1, v2, s[60:61] offset:2816
.Lxb_done_0:
	s_waitcnt vmcnt(0)
	buffer_inv sc1
	s_waitcnt vmcnt(0)

.LBB0_224:
	s_or_b64 exec, exec, s[8:9]
	v_cvt_f32_u32_e32 v5, v3
	s_waitcnt vmcnt(0)
	v_readfirstlane_b32 s3, v4
	v_sub_u32_e32 v4, 0, v3
	v_rcp_iflag_f32_e32 v5, v5
	v_add_u32_e32 v6, s3, v2
	v_mul_f32_e32 v5, 0x4f7ffffe, v5
	v_cvt_u32_f32_e32 v5, v5
	v_mul_lo_u32 v2, v4, v5
	v_mul_hi_u32 v2, v5, v2
	v_add_u32_e32 v2, v5, v2
	v_mul_hi_u32 v2, v6, v2
	v_mul_lo_u32 v4, v2, v3
	v_sub_u32_e32 v4, v6, v4
	v_add_u32_e32 v5, 1, v2
	v_cmp_ge_u32_e32 vcc, v4, v3
	s_nop 1
	v_cndmask_b32_e32 v2, v2, v5, vcc
	v_sub_u32_e32 v5, v4, v3
	v_cndmask_b32_e32 v4, v4, v5, vcc
	v_add_u32_e32 v5, 1, v2
	v_cmp_ge_u32_e32 vcc, v4, v3
	v_add_u32_e32 v4, 1, v6
	s_nop 0
	v_cndmask_b32_e32 v2, v2, v5, vcc
	v_mul_lo_u32 v5, v3, v2
	v_add_u32_e32 v3, v5, v3
	v_cmp_ne_u32_e32 vcc, v4, v3
	v_readfirstlane_b32 s98, v2
	s_and_saveexec_b64 s[6:7], vcc
	s_xor_b64 s[6:7], exec, s[6:7]
	s_cbranch_execz .LBB0_238
	s_waitcnt lgkmcnt(0)
	v_mov_b32_e32 v1, 0x2000
	global_load_dword v1, v1, s[4:5] offset:1024 sc1
	s_add_u32 s10, s4, 0x2400
	s_addc_u32 s11, s5, 0
	s_waitcnt vmcnt(0)
	v_cmp_eq_u32_e32 vcc, v1, v2
	s_and_saveexec_b64 s[8:9], vcc
	s_cbranch_execz .LBB0_237
	s_mov_b32 s3, 1
	s_mov_b64 s[16:17], 0
	v_mov_b32_e32 v1, 0
	s_branch .LBB0_228

.LBB0_241:
	s_or_b64 exec, exec, s[8:9]
	v_cvt_f32_u32_e32 v4, v1
	s_waitcnt vmcnt(0)
	v_readfirstlane_b32 s3, v3
	s_add_u32 s8, s60, 0x3500
	s_addc_u32 s9, s61, 0
	v_rcp_iflag_f32_e32 v4, v4
	v_add_u32_e32 v2, s3, v2
	v_add_u32_e32 v5, 1, v2
	s_mov_b64 s[10:11], -1
	v_mul_f32_e32 v3, 0x4f7ffffe, v4
	v_cvt_u32_f32_e32 v3, v3
	v_sub_u32_e32 v4, 0, v1
	v_mul_lo_u32 v4, v4, v3
	v_mul_hi_u32 v4, v3, v4
	v_add_u32_e32 v3, v3, v4
	v_mul_hi_u32 v3, v2, v3
	v_mul_lo_u32 v4, v3, v1
	v_sub_u32_e32 v2, v2, v4
	v_add_u32_e32 v6, 1, v3
	v_cmp_ge_u32_e32 vcc, v2, v1
	v_sub_u32_e32 v4, v2, v1
	s_nop 0
	v_cndmask_b32_e32 v3, v3, v6, vcc
	v_cndmask_b32_e32 v2, v2, v4, vcc
	v_add_u32_e32 v4, 1, v3
	v_cmp_ge_u32_e32 vcc, v2, v1
	s_nop 1
	v_cndmask_b32_e32 v4, v3, v4, vcc
	v_mul_lo_u32 v2, v1, v4
	v_add_u32_e32 v1, v2, v1
	v_cmp_ne_u32_e32 vcc, v5, v1
	v_mov_b64_e32 v[2:3], s[8:9]
	s_and_b64 vcc, exec, vcc
	s_cbranch_vccz .Lxb_last_1
	v_mov_b32_e32 v1, 0x2000
	s_mov_b32 s99, 0
.Lxb_spin_1:
	global_load_dword v2, v1, s[4:5] offset:1024 sc1
	s_add_u32 s99, s99, 1
	s_waitcnt vmcnt(0)
	v_readfirstlane_b32 s100, v2
	s_cmp_lg_u32 s100, s98
	s_cbranch_scc1 .Lxb_done_1
	s_cmp_gt_u32 s99, 0x40000
	s_cbranch_scc1 .Lxb_done_1
	s_sleep 1
	s_branch .Lxb_spin_1

.LBB0_761:
	s_or_b64 exec, exec, s[8:9]
	v_cvt_f32_u32_e32 v5, v3
	s_waitcnt vmcnt(0)
	v_readfirstlane_b32 s3, v4
	v_sub_u32_e32 v4, 0, v3
	v_rcp_iflag_f32_e32 v5, v5
	v_add_u32_e32 v6, s3, v2
	v_mul_f32_e32 v5, 0x4f7ffffe, v5
	v_cvt_u32_f32_e32 v5, v5
	v_mul_lo_u32 v2, v4, v5
	v_mul_hi_u32 v2, v5, v2
	v_add_u32_e32 v2, v5, v2
	v_mul_hi_u32 v2, v6, v2
	v_mul_lo_u32 v4, v2, v3
	v_sub_u32_e32 v4, v6, v4
	v_add_u32_e32 v5, 1, v2
	v_cmp_ge_u32_e32 vcc, v4, v3
	s_nop 1
	v_cndmask_b32_e32 v2, v2, v5, vcc
	v_sub_u32_e32 v5, v4, v3
	v_cndmask_b32_e32 v4, v4, v5, vcc
	v_add_u32_e32 v5, 1, v2
	v_cmp_ge_u32_e32 vcc, v4, v3
	v_add_u32_e32 v4, 1, v6
	s_nop 0
	v_cndmask_b32_e32 v2, v2, v5, vcc
	v_mul_lo_u32 v5, v3, v2
	v_add_u32_e32 v3, v5, v3
	v_cmp_ne_u32_e32 vcc, v4, v3
	v_readfirstlane_b32 s98, v2
	s_and_saveexec_b64 s[6:7], vcc
	s_xor_b64 s[6:7], exec, s[6:7]
	s_cbranch_execz .LBB0_775
	s_waitcnt lgkmcnt(0)
	v_mov_b32_e32 v1, 0x2000
	global_load_dword v1, v1, s[4:5] offset:1024 sc1
	s_add_u32 s10, s4, 0x2400
	s_addc_u32 s11, s5, 0
	s_waitcnt vmcnt(0)
	v_cmp_eq_u32_e32 vcc, v1, v2
	s_and_saveexec_b64 s[8:9], vcc
	s_cbranch_execz .LBB0_774
	s_mov_b32 s3, 1
	s_mov_b64 s[12:13], 0
	v_mov_b32_e32 v1, 0
	s_branch .LBB0_765

.LBB0_1277:
	s_or_b64 exec, exec, s[6:7]
	v_cvt_f32_u32_e32 v5, v3
	s_waitcnt vmcnt(0)
	v_readfirstlane_b32 s4, v4
	v_sub_u32_e32 v4, 0, v3
	v_rcp_iflag_f32_e32 v5, v5
	v_add_u32_e32 v6, s4, v2
	v_mul_f32_e32 v5, 0x4f7ffffe, v5
	v_cvt_u32_f32_e32 v5, v5
	v_mul_lo_u32 v2, v4, v5
	v_mul_hi_u32 v2, v5, v2
	v_add_u32_e32 v2, v5, v2
	v_mul_hi_u32 v2, v6, v2
	v_mul_lo_u32 v4, v2, v3
	v_sub_u32_e32 v4, v6, v4
	v_add_u32_e32 v5, 1, v2
	v_cmp_ge_u32_e32 vcc, v4, v3
	s_nop 1
	v_cndmask_b32_e32 v2, v2, v5, vcc
	v_sub_u32_e32 v5, v4, v3
	v_cndmask_b32_e32 v4, v4, v5, vcc
	v_add_u32_e32 v5, 1, v2
	v_cmp_ge_u32_e32 vcc, v4, v3
	v_add_u32_e32 v4, 1, v6
	s_nop 0
	v_cndmask_b32_e32 v2, v2, v5, vcc
	v_mul_lo_u32 v5, v3, v2
	v_add_u32_e32 v3, v5, v3
	v_cmp_ne_u32_e32 vcc, v4, v3
	v_readfirstlane_b32 s98, v2
	s_and_saveexec_b64 s[4:5], vcc
	s_xor_b64 s[4:5], exec, s[4:5]
	s_cbranch_execz .LBB0_1291
	s_waitcnt lgkmcnt(0)
	v_mov_b32_e32 v1, 0x2000
	global_load_dword v1, v1, s[2:3] offset:1024 sc1
	s_add_u32 s8, s2, 0x2400
	s_addc_u32 s9, s3, 0
	s_waitcnt vmcnt(0)
	v_cmp_eq_u32_e32 vcc, v1, v2
	s_and_saveexec_b64 s[6:7], vcc
	s_cbranch_execz .LBB0_1290
	s_mov_b32 s20, 1
	s_mov_b64 s[10:11], 0
	v_mov_b32_e32 v1, 0
	s_branch .LBB0_1281

.LBB0_1294:
	s_or_b64 exec, exec, s[6:7]
	v_cvt_f32_u32_e32 v4, v1
	s_waitcnt vmcnt(0)
	v_readfirstlane_b32 s4, v3
	s_add_u32 s6, s60, 0x3500
	s_addc_u32 s7, s61, 0
	v_rcp_iflag_f32_e32 v4, v4
	v_add_u32_e32 v2, s4, v2
	v_add_u32_e32 v5, 1, v2
	s_mov_b64 s[8:9], -1
	v_mul_f32_e32 v3, 0x4f7ffffe, v4
	v_cvt_u32_f32_e32 v3, v3
	v_sub_u32_e32 v4, 0, v1
	v_mul_lo_u32 v4, v4, v3
	v_mul_hi_u32 v4, v3, v4
	v_add_u32_e32 v3, v3, v4
	v_mul_hi_u32 v3, v2, v3
	v_mul_lo_u32 v4, v3, v1
	v_sub_u32_e32 v2, v2, v4
	v_add_u32_e32 v6, 1, v3
	v_cmp_ge_u32_e32 vcc, v2, v1
	v_sub_u32_e32 v4, v2, v1
	s_nop 0
	v_cndmask_b32_e32 v3, v3, v6, vcc
	v_cndmask_b32_e32 v2, v2, v4, vcc
	v_add_u32_e32 v4, 1, v3
	v_cmp_ge_u32_e32 vcc, v2, v1
	s_nop 1
	v_cndmask_b32_e32 v4, v3, v4, vcc
	v_mul_lo_u32 v2, v1, v4
	v_add_u32_e32 v1, v2, v1
	v_cmp_ne_u32_e32 vcc, v5, v1
	v_mov_b64_e32 v[2:3], s[6:7]
	s_and_b64 vcc, exec, vcc
	s_cbranch_vccz .Lxb_last_11
	v_mov_b32_e32 v1, 0x2000
	s_mov_b32 s99, 0
.Lxb_spin_11:
	global_load_dword v2, v1, s[2:3] offset:1024 sc1
	s_add_u32 s99, s99, 1
	s_waitcnt vmcnt(0)
	v_readfirstlane_b32 s100, v2
	s_cmp_lg_u32 s100, s98
	s_cbranch_scc1 .Lxb_done_11
	s_cmp_gt_u32 s99, 0x40000
	s_cbranch_scc1 .Lxb_done_11
	s_sleep 1
	s_branch .Lxb_spin_11
